# speedup vs baseline: 1.0180x; 1.0180x over previous
.LBB2_124:
	s_or_b64 exec, exec, s[76:77]
	s_load_dwordx4 s[76:79], s[0:1], 0x28
	s_waitcnt lgkmcnt(0)
	s_barrier
	ds_read_b32 v6, v8 offset:1024
	v_mov_b32_e32 v4, 0
	v_mov_b32_e32 v5, 0
	s_waitcnt lgkmcnt(0)
	ds_write_b32 v8, v6
	s_waitcnt lgkmcnt(0)
	s_barrier
	s_and_saveexec_b64 s[0:1], vcc
	ds_read_b32 v5, v51
	s_or_b64 exec, exec, s[0:1]
	s_waitcnt lgkmcnt(0)
	s_barrier
	ds_read_b32 v7, v8
	s_waitcnt lgkmcnt(0)
	v_add_u32_e32 v5, v7, v5
	ds_write_b32 v8, v5
	s_waitcnt lgkmcnt(0)
	s_barrier
	s_and_saveexec_b64 s[0:1], s[52:53]
	ds_read_b32 v4, v52
	s_or_b64 exec, exec, s[0:1]
	s_waitcnt lgkmcnt(0)
	s_barrier
	ds_read_b32 v5, v8
	s_waitcnt lgkmcnt(0)
	v_add_u32_e32 v4, v5, v4
	ds_write_b32 v8, v4
	v_mov_b32_e32 v4, 0
	v_mov_b32_e32 v5, 0
	s_waitcnt lgkmcnt(0)
	s_barrier
	s_and_saveexec_b64 s[0:1], s[54:55]
	ds_read_b32 v5, v53
	s_or_b64 exec, exec, s[0:1]
	s_waitcnt lgkmcnt(0)
	s_barrier
	ds_read_b32 v7, v8
	s_waitcnt lgkmcnt(0)
	v_add_u32_e32 v5, v7, v5
	ds_write_b32 v8, v5
	s_waitcnt lgkmcnt(0)
	s_barrier
	s_and_saveexec_b64 s[0:1], s[56:57]
	ds_read_b32 v4, v54
	s_or_b64 exec, exec, s[0:1]
	s_waitcnt lgkmcnt(0)
	s_barrier
	ds_read_b32 v5, v8
	s_waitcnt lgkmcnt(0)
	v_add_u32_e32 v4, v5, v4
	ds_write_b32 v8, v4
	v_mov_b32_e32 v4, 0
	v_mov_b32_e32 v5, 0
	s_waitcnt lgkmcnt(0)
	s_barrier
	s_and_saveexec_b64 s[0:1], s[58:59]
	ds_read_b32 v5, v55
	s_or_b64 exec, exec, s[0:1]
	s_waitcnt lgkmcnt(0)
	s_barrier
	ds_read_b32 v7, v8
	s_waitcnt lgkmcnt(0)
	v_add_u32_e32 v5, v7, v5
	ds_write_b32 v8, v5
	s_waitcnt lgkmcnt(0)
	s_barrier
	s_and_saveexec_b64 s[0:1], s[60:61]
	v_add_u32_e32 v4, 0xffffff80, v8
	ds_read_b32 v4, v4
	s_or_b64 exec, exec, s[0:1]
	s_waitcnt lgkmcnt(0)
	s_barrier
	ds_read_b32 v5, v8
	s_waitcnt lgkmcnt(0)
	v_add_u32_e32 v4, v5, v4
	ds_write_b32 v8, v4
	v_mov_b32_e32 v4, 0
	v_mov_b32_e32 v5, 0
	s_waitcnt lgkmcnt(0)
	s_barrier
	s_and_saveexec_b64 s[0:1], s[62:63]
	v_add_u32_e32 v5, 0xffffff00, v8
	ds_read_b32 v5, v5
	s_or_b64 exec, exec, s[0:1]
	s_waitcnt lgkmcnt(0)
	s_barrier
	ds_read_b32 v7, v8
	s_waitcnt lgkmcnt(0)
	v_add_u32_e32 v5, v7, v5
	ds_write_b32 v8, v5
	s_waitcnt lgkmcnt(0)
	s_barrier
	s_and_saveexec_b64 s[0:1], s[64:65]
	v_add_u32_e32 v4, 0xfffffe00, v8
	ds_read_b32 v4, v4
	s_or_b64 exec, exec, s[0:1]
	s_waitcnt lgkmcnt(0)
	s_barrier
	ds_read_b32 v5, v8
	s_lshl_b32 s33, s2, 8
	s_mov_b32 s0, 0x186a0
	s_waitcnt lgkmcnt(0)
	v_add_u32_e32 v4, v5, v4
	ds_write_b32 v8, v4
	s_waitcnt lgkmcnt(0)
	s_barrier
	ds_read_b32 v7, v8
	v_or_b32_e32 v4, s33, v0
	v_cmp_lt_u32_e32 vcc, s0, v4
	s_waitcnt lgkmcnt(0)
	s_barrier
	v_sub_u32_e32 v51, v7, v6
	v_add_u32_e32 v52, v51, v2
	s_and_saveexec_b64 s[0:1], vcc
	s_xor_b64 s[0:1], exec, s[0:1]
	v_add_u32_e32 v52, v51, v2
	s_andn2_saveexec_b64 s[0:1], s[0:1]
	s_cbranch_execz .LBB2_144
